# v15 + E4b token loop: the four y-row loads (independent of routing data) issued at the top of the iteration, vmcnt ladder re-derived
# speedup vs baseline: 1.0052x; 1.0052x over previous
; template <class T> __device__ __forceinline__ T* wsp(const Frame& F, size_t off) { return (T*)(F.ws + off); }
; __device__ __forceinline__ void phase_e4(Frame& F, int layer, int chunk, int CT, bool dry = false) {
;     ...
;         f32x4 y[4], v[4]; ldrow_fp8(YE + ((size_t)256 * NBr + (t - cstart)) * DM, F.lane, y);
; #pragma unroll
;         for (int k = 0; k < TOPK; ++k) { const int s = __builtin_amdgcn_readfirstlane(TS[t * 8 + k]); const float gt = __builtin_bit_cast(float, __builtin_amdgcn_readfirstlane(__builtin_bit_cast(int, TG[t * 8 + k])));
;             const size_t row = (size_t)256 * tbs[s >> 20] + (s & 0xfffff); ldrow_fp8(YE + row * DM, F.lane, v);
; #pragma unroll
;             for (int j = 0; j < 4; ++j) y[j] = y[j] + v[j] * gt; }
;         float* xo = t < TL ? F.out + (size_t)t * DM : wsp<float>(F, WS_CTXRES) + (size_t)(t - TL) * DM;
;         f32x4 x[4];
;         if (X1_RECOMPUTE && KSPLIT_CTX && layer == 0 && t < TL) { f32x4 y1[4]; ldrow_f32_nt(inp(F, I_X) + (size_t)t * DM, F.lane, x); ldrow_bf16_nt((const bf16*)F.out + (size_t)t * 2048, F.lane, y1);
;             const float ry1 = rstd_of(y1);
; #pragma unroll
;             for (int j = 0; j < 4; ++j) x[j] = x[j] + (y1[j] * ry1) * C1[j]; }
;         else if (layer == 0 || !X3_BF16) ldrow_f32_nt(xo, F.lane, x); else ldrow_bf16_nt((const bf16*)xo, F.lane, x);
.LBB0_1809:
	s_ashr_i32 s11, s10, 31
	s_lshl_b64 s[22:23], s[10:11], 2
	s_add_u32 s44, s34, s22
	s_addc_u32 s45, s36, s23
	global_load_dwordx4 v[42:45], v27, s[44:45]
	global_load_dwordx2 v[34:35], v27, s[44:45] offset:16
	s_add_u32 s22, s37, s22
	s_addc_u32 s23, s40, s23
	global_load_dwordx4 v[16:19], v27, s[22:23]
	v_lshlrev_b32_e32 v128, 3, v24
	global_load_dwordx2 v[120:121], v128, s[12:13] nt
	global_load_dwordx2 v[122:123], v128, s[12:13] offset:512 nt
	global_load_dwordx2 v[124:125], v128, s[12:13] offset:1024 nt
	global_load_dwordx2 v[126:127], v128, s[12:13] offset:1536 nt
	v_readfirstlane_b32 s44, v30
	v_readfirstlane_b32 s45, v31
	s_add_i32 s2, s2, 1
	s_add_i32 s10, s10, 8
	v_lshl_add_u64 v[30:31], v[30:31], 0, s[20:21]
	s_waitcnt vmcnt(6)
	v_readfirstlane_b32 s4, v42
	global_load_dwordx4 v[20:23], v32, s[44:45] nt
	v_readfirstlane_b32 s24, v44
	v_readfirstlane_b32 s11, v43
	v_readfirstlane_b32 s30, v45
	s_waitcnt vmcnt(6)
	v_readfirstlane_b32 s31, v34
	v_readfirstlane_b32 s46, v35
	s_ashr_i32 s44, s4, 20
	s_ashr_i32 s47, s24, 20
	s_ashr_i32 s45, s11, 20
	s_ashr_i32 s48, s30, 20
	s_ashr_i32 s49, s31, 20
	s_ashr_i32 s50, s46, 20
	s_lshl_b32 s44, s44, 2
	s_lshl_b32 s47, s47, 2
	s_lshl_b32 s45, s45, 2
	s_lshl_b32 s48, s48, 2
	s_lshl_b32 s49, s49, 2
	s_lshl_b32 s50, s50, 2
	s_add_i32 s44, s38, s44
	s_add_i32 s47, s38, s47
	s_add_i32 s45, s38, s45
	s_add_i32 s48, s38, s48
	s_add_i32 s49, s38, s49
	s_add_i32 s50, s38, s50
	v_mov_b32_e32 v26, s44
	v_mov_b32_e32 v35, s47
	v_mov_b32_e32 v33, s45
	v_mov_b32_e32 v42, s48
	v_mov_b32_e32 v43, s49
	v_mov_b32_e32 v44, s50
	ds_read_b32 v34, v26
	ds_read_b32 v46, v33
	ds_read_b32 v50, v35
	ds_read_b32 v54, v42
	ds_read_b32 v56, v43
	ds_read_b32 v58, v44
	s_waitcnt lgkmcnt(5)
	v_ashrrev_i32_e32 v35, 31, v34
	s_lshl_b32 s4, s4, 10
	v_lshlrev_b64 v[34:35], 18, v[34:35]
	s_and_b32 s4, s4, 0x3ffffc00
	v_lshl_add_u64 v[34:35], s[8:9], 0, v[34:35]
	v_lshl_add_u64 v[34:35], v[34:35], 0, s[4:5]
	s_waitcnt lgkmcnt(4)
	v_ashrrev_i32_e32 v47, 31, v46
	s_lshl_b32 s11, s11, 10
	v_readfirstlane_b32 s44, v34
	v_readfirstlane_b32 s45, v35
	v_lshlrev_b64 v[34:35], 18, v[46:47]
	v_lshl_add_u64 v[34:35], s[8:9], 0, v[34:35]
	s_and_b32 s4, s11, 0x3ffffc00
	v_lshl_add_u64 v[34:35], v[34:35], 0, s[4:5]
	s_waitcnt lgkmcnt(3)
	v_ashrrev_i32_e32 v51, 31, v50
	s_lshl_b32 s24, s24, 10
	global_load_dwordx4 v[42:45], v32, s[44:45] nt
	v_readfirstlane_b32 s44, v34
	v_readfirstlane_b32 s45, v35
	v_lshlrev_b64 v[34:35], 18, v[50:51]
	v_lshl_add_u64 v[34:35], s[8:9], 0, v[34:35]
	s_and_b32 s4, s24, 0x3ffffc00
	v_lshl_add_u64 v[34:35], v[34:35], 0, s[4:5]
	s_waitcnt lgkmcnt(2)
	v_ashrrev_i32_e32 v55, 31, v54
	global_load_dwordx4 v[46:49], v32, s[44:45] nt
	v_readfirstlane_b32 s44, v34
	v_readfirstlane_b32 s45, v35
	s_nop 4
	global_load_dwordx4 v[50:53], v32, s[44:45] nt
	global_load_dwordx2 v[34:35], v27, s[22:23] offset:16
	s_lshl_b32 s4, s30, 10
	s_waitcnt vmcnt(9)
	v_readfirstlane_b32 s44, v16
	v_readfirstlane_b32 s24, v17
	v_lshlrev_b64 v[16:17], 18, v[54:55]
	s_waitcnt lgkmcnt(1)
	v_ashrrev_i32_e32 v57, 31, v56
	v_lshl_add_u64 v[16:17], s[8:9], 0, v[16:17]
	s_and_b32 s4, s4, 0x3ffffc00
	s_lshl_b32 s11, s31, 10
	s_waitcnt lgkmcnt(0)
	v_ashrrev_i32_e32 v59, 31, v58
	v_lshl_add_u64 v[16:17], v[16:17], 0, s[4:5]
	s_lshl_b32 s23, s46, 10
	s_and_b32 s4, s11, 0x3ffffc00
	v_readfirstlane_b32 s46, v16
	v_readfirstlane_b32 s47, v17
	v_readfirstlane_b32 s22, v18
	v_lshlrev_b32_e32 v26, 3, v24
	s_waitcnt vmcnt(4)
	v_cvt_pk_f32_fp8_e32 v[62:63], v20
	v_cvt_pk_f32_fp8_sdwa v[64:65], v20 src0_sel:WORD_1
	v_cvt_pk_f32_fp8_e32 v[66:67], v21
	v_cvt_pk_f32_fp8_sdwa v[68:69], v21 src0_sel:WORD_1
	v_lshlrev_b64 v[20:21], 18, v[56:57]
	v_cvt_pk_f32_fp8_e32 v[70:71], v22
	v_cvt_pk_f32_fp8_sdwa v[72:73], v22 src0_sel:WORD_1
	v_cvt_pk_f32_fp8_e32 v[74:75], v23
	v_cvt_pk_f32_fp8_sdwa v[76:77], v23 src0_sel:WORD_1
	v_lshlrev_b64 v[22:23], 18, v[58:59]
	v_lshl_add_u64 v[20:21], s[8:9], 0, v[20:21]
	v_lshl_add_u64 v[54:55], s[8:9], 0, v[22:23]
	v_lshl_add_u64 v[16:17], v[20:21], 0, s[4:5]
	global_load_dwordx4 v[20:23], v32, s[46:47] nt
	s_and_b32 s4, s23, 0x3ffffc00
	v_readfirstlane_b32 s46, v16
	v_readfirstlane_b32 s47, v17
	v_lshl_add_u64 v[16:17], v[54:55], 0, s[4:5]
	v_readfirstlane_b32 s4, v19
	v_readfirstlane_b32 s48, v16
	v_readfirstlane_b32 s49, v17
	s_nop 0
	global_load_dwordx4 v[54:57], v32, s[46:47] nt
	s_nop 2
	global_load_dwordx4 v[58:61], v32, s[48:49] nt
	s_waitcnt vmcnt(6)
	v_cvt_pk_f32_fp8_e32 v[82:83], v44
	v_cvt_pk_f32_fp8_sdwa v[84:85], v44 src0_sel:WORD_1
	v_cvt_pk_f32_fp8_e32 v[86:87], v45
	v_cvt_pk_f32_fp8_sdwa v[44:45], v45 src0_sel:WORD_1
	v_cvt_pk_f32_fp8_e32 v[16:17], v42
	v_cvt_pk_f32_fp8_sdwa v[78:79], v42 src0_sel:WORD_1
	v_cvt_pk_f32_fp8_e32 v[80:81], v43
	v_cvt_pk_f32_fp8_sdwa v[42:43], v43 src0_sel:WORD_1
	s_waitcnt vmcnt(5)
	v_cvt_pk_f32_fp8_e32 v[94:95], v48
	v_cvt_pk_f32_fp8_sdwa v[96:97], v48 src0_sel:WORD_1
	v_cvt_pk_f32_fp8_e32 v[98:99], v49
	v_cvt_pk_f32_fp8_sdwa v[48:49], v49 src0_sel:WORD_1
	v_cvt_pk_f32_fp8_e32 v[88:89], v46
	v_cvt_pk_f32_fp8_sdwa v[90:91], v46 src0_sel:WORD_1
	v_cvt_pk_f32_fp8_e32 v[92:93], v47
	v_cvt_pk_f32_fp8_sdwa v[46:47], v47 src0_sel:WORD_1
	s_waitcnt vmcnt(4)
; __device__ __forceinline__ void phase_e4(Frame& F, int layer, int chunk, int CT, bool dry = false) {
;     ...
;         f32x4 y[4], v[4]; ldrow_fp8(YE + ((size_t)256 * NBr + (t - cstart)) * DM, F.lane, y);
; #pragma unroll
;         for (int k = 0; k < TOPK; ++k) { const int s = __builtin_amdgcn_readfirstlane(TS[t * 8 + k]); const float gt = __builtin_bit_cast(float, __builtin_amdgcn_readfirstlane(__builtin_bit_cast(int, TG[t * 8 + k])));
;             const size_t row = (size_t)256 * tbs[s >> 20] + (s & 0xfffff); ldrow_fp8(YE + row * DM, F.lane, v);
; #pragma unroll
;             for (int j = 0; j < 4; ++j) y[j] = y[j] + v[j] * gt; }
	v_cvt_pk_f32_fp8_e32 v[106:107], v52
	v_cvt_pk_f32_fp8_sdwa v[108:109], v52 src0_sel:WORD_1
	v_cvt_pk_f32_fp8_e32 v[110:111], v53
	v_cvt_pk_f32_fp8_sdwa v[52:53], v53 src0_sel:WORD_1
	v_cvt_pk_f32_fp8_e32 v[100:101], v50
	v_cvt_pk_f32_fp8_sdwa v[102:103], v50 src0_sel:WORD_1
	v_cvt_pk_f32_fp8_e32 v[104:105], v51
	v_cvt_pk_f32_fp8_sdwa v[50:51], v51 src0_sel:WORD_1
	v_pk_mul_f32 v[44:45], v[44:45], s[18:19] op_sel_hi:[1,0]
	v_pk_mul_f32 v[16:17], v[16:17], s[18:19] op_sel_hi:[1,0]
	v_pk_mul_f32 v[42:43], v[42:43], s[18:19] op_sel_hi:[1,0]
	v_pk_mul_f32 v[80:81], v[80:81], s[18:19] op_sel_hi:[1,0]
	v_pk_mul_f32 v[82:83], v[82:83], s[18:19] op_sel_hi:[1,0]
	v_pk_mul_f32 v[44:45], s[44:45], v[44:45] op_sel_hi:[0,1]
	v_pk_mul_f32 v[84:85], v[84:85], s[18:19] op_sel_hi:[1,0]
	v_pk_mul_f32 v[86:87], v[86:87], s[18:19] op_sel_hi:[1,0]
	v_pk_mul_f32 v[16:17], s[44:45], v[16:17] op_sel_hi:[0,1]
	v_pk_mul_f32 v[80:81], s[44:45], v[80:81] op_sel_hi:[0,1]
	v_pk_mul_f32 v[42:43], s[44:45], v[42:43] op_sel_hi:[0,1]
	v_pk_mul_f32 v[82:83], s[44:45], v[82:83] op_sel_hi:[0,1]
	v_pk_mul_f32 v[48:49], v[48:49], s[18:19] op_sel_hi:[1,0]
	v_pk_fma_f32 v[44:45], v[76:77], s[18:19], v[44:45] op_sel_hi:[1,0,1]
	v_pk_mul_f32 v[84:85], s[44:45], v[84:85] op_sel_hi:[0,1]
	v_pk_mul_f32 v[86:87], s[44:45], v[86:87] op_sel_hi:[0,1]
	v_pk_mul_f32 v[88:89], v[88:89], s[18:19] op_sel_hi:[1,0]
	v_pk_mul_f32 v[46:47], v[46:47], s[18:19] op_sel_hi:[1,0]
	v_pk_mul_f32 v[92:93], v[92:93], s[18:19] op_sel_hi:[1,0]
	v_pk_mul_f32 v[94:95], v[94:95], s[18:19] op_sel_hi:[1,0]
	v_pk_fma_f32 v[16:17], v[62:63], s[18:19], v[16:17] op_sel_hi:[1,0,1]
	v_pk_fma_f32 v[42:43], v[68:69], s[18:19], v[42:43] op_sel_hi:[1,0,1]
	v_pk_fma_f32 v[62:63], v[66:67], s[18:19], v[80:81] op_sel_hi:[1,0,1]
	v_pk_fma_f32 v[66:67], v[70:71], s[18:19], v[82:83] op_sel_hi:[1,0,1]
	v_pk_mul_f32 v[52:53], v[52:53], s[18:19] op_sel_hi:[1,0]
	v_pk_fma_f32 v[44:45], s[24:25], v[48:49], v[44:45] op_sel_hi:[0,1,1]
	v_pk_mul_f32 v[96:97], v[96:97], s[18:19] op_sel_hi:[1,0]
	v_pk_mul_f32 v[98:99], v[98:99], s[18:19] op_sel_hi:[1,0]
	v_pk_fma_f32 v[68:69], v[72:73], s[18:19], v[84:85] op_sel_hi:[1,0,1]
	v_pk_fma_f32 v[70:71], v[74:75], s[18:19], v[86:87] op_sel_hi:[1,0,1]
	v_pk_mul_f32 v[72:73], v[100:101], s[18:19] op_sel_hi:[1,0]
	v_pk_mul_f32 v[76:77], v[104:105], s[18:19] op_sel_hi:[1,0]
	v_pk_mul_f32 v[50:51], v[50:51], s[18:19] op_sel_hi:[1,0]
	v_pk_mul_f32 v[80:81], v[106:107], s[18:19] op_sel_hi:[1,0]
	v_pk_fma_f32 v[16:17], s[24:25], v[88:89], v[16:17] op_sel_hi:[0,1,1]
	v_pk_fma_f32 v[62:63], s[24:25], v[92:93], v[62:63] op_sel_hi:[0,1,1]
	v_pk_fma_f32 v[42:43], s[24:25], v[46:47], v[42:43] op_sel_hi:[0,1,1]
	v_pk_fma_f32 v[66:67], s[24:25], v[94:95], v[66:67] op_sel_hi:[0,1,1]
	v_pk_fma_f32 v[44:45], s[22:23], v[52:53], v[44:45] op_sel_hi:[0,1,1]
	s_waitcnt vmcnt(2)
	v_cvt_pk_f32_fp8_e32 v[52:53], v20
	v_pk_mul_f32 v[78:79], v[78:79], s[18:19] op_sel_hi:[1,0]
	v_pk_fma_f32 v[46:47], s[24:25], v[96:97], v[68:69] op_sel_hi:[0,1,1]
	v_pk_fma_f32 v[48:49], s[24:25], v[98:99], v[70:71] op_sel_hi:[0,1,1]
	v_pk_fma_f32 v[16:17], s[22:23], v[72:73], v[16:17] op_sel_hi:[0,1,1]
	v_pk_fma_f32 v[42:43], s[22:23], v[50:51], v[42:43] op_sel_hi:[0,1,1]
	v_pk_fma_f32 v[50:51], s[22:23], v[76:77], v[62:63] op_sel_hi:[0,1,1]
	v_pk_fma_f32 v[62:63], s[22:23], v[80:81], v[66:67] op_sel_hi:[0,1,1]
	v_cvt_pk_f32_fp8_sdwa v[18:19], v20 src0_sel:WORD_1
	v_cvt_pk_f32_fp8_sdwa v[66:67], v21 src0_sel:WORD_1
	v_cvt_pk_f32_fp8_e32 v[20:21], v21
	v_cvt_pk_f32_fp8_e32 v[68:69], v22
	v_cvt_pk_f32_fp8_sdwa v[70:71], v22 src0_sel:WORD_1
	v_cvt_pk_f32_fp8_e32 v[72:73], v23
	v_cvt_pk_f32_fp8_sdwa v[22:23], v23 src0_sel:WORD_1
	v_pk_mul_f32 v[78:79], s[44:45], v[78:79] op_sel_hi:[0,1]
	v_pk_mul_f32 v[90:91], v[90:91], s[18:19] op_sel_hi:[1,0]
	v_pk_fma_f32 v[64:65], v[64:65], s[18:19], v[78:79] op_sel_hi:[1,0,1]
	v_pk_mul_f32 v[74:75], v[102:103], s[18:19] op_sel_hi:[1,0]
	v_pk_mul_f32 v[82:83], v[110:111], s[18:19] op_sel_hi:[1,0]
	v_pk_fma_f32 v[64:65], s[24:25], v[90:91], v[64:65] op_sel_hi:[0,1,1]
	v_pk_mul_f32 v[52:53], v[52:53], s[18:19] op_sel_hi:[1,0]
	v_pk_fma_f32 v[64:65], s[22:23], v[74:75], v[64:65] op_sel_hi:[0,1,1]
	v_pk_fma_f32 v[48:49], s[22:23], v[82:83], v[48:49] op_sel_hi:[0,1,1]
	v_pk_mul_f32 v[18:19], v[18:19], s[18:19] op_sel_hi:[1,0]
	v_pk_mul_f32 v[66:67], v[66:67], s[18:19] op_sel_hi:[1,0]
	v_pk_mul_f32 v[20:21], v[20:21], s[18:19] op_sel_hi:[1,0]
	v_pk_mul_f32 v[68:69], v[68:69], s[18:19] op_sel_hi:[1,0]
	v_pk_mul_f32 v[72:73], v[72:73], s[18:19] op_sel_hi:[1,0]
	v_pk_mul_f32 v[22:23], v[22:23], s[18:19] op_sel_hi:[1,0]
	v_pk_fma_f32 v[16:17], s[4:5], v[52:53], v[16:17] op_sel_hi:[0,1,1]
	s_waitcnt vmcnt(1)
	v_cvt_pk_f32_fp8_sdwa v[52:53], v54 src0_sel:WORD_1
	v_pk_fma_f32 v[18:19], s[4:5], v[18:19], v[64:65] op_sel_hi:[0,1,1]
	v_pk_fma_f32 v[20:21], s[4:5], v[20:21], v[50:51] op_sel_hi:[0,1,1]
	v_pk_fma_f32 v[42:43], s[4:5], v[66:67], v[42:43] op_sel_hi:[0,1,1]
	v_pk_fma_f32 v[50:51], s[4:5], v[68:69], v[62:63] op_sel_hi:[0,1,1]
	v_pk_fma_f32 v[22:23], s[4:5], v[22:23], v[44:45] op_sel_hi:[0,1,1]
	v_pk_fma_f32 v[44:45], s[4:5], v[72:73], v[48:49] op_sel_hi:[0,1,1]
	v_cvt_pk_f32_fp8_e32 v[48:49], v54
	v_cvt_pk_f32_fp8_sdwa v[64:65], v56 src0_sel:WORD_1
	v_cvt_pk_f32_fp8_e32 v[66:67], v56
	v_cvt_pk_f32_fp8_sdwa v[68:69], v57 src0_sel:WORD_1
	v_cvt_pk_f32_fp8_e32 v[56:57], v57
	v_pk_mul_f32 v[78:79], v[108:109], s[18:19] op_sel_hi:[1,0]
	v_pk_mul_f32 v[70:71], v[70:71], s[18:19] op_sel_hi:[1,0]
	v_pk_fma_f32 v[46:47], s[22:23], v[78:79], v[46:47] op_sel_hi:[0,1,1]
	v_pk_fma_f32 v[46:47], s[4:5], v[70:71], v[46:47] op_sel_hi:[0,1,1]
	v_readfirstlane_b32 s4, v34
	v_pk_mul_f32 v[52:53], v[52:53], s[18:19] op_sel_hi:[1,0]
	v_pk_mul_f32 v[48:49], v[48:49], s[18:19] op_sel_hi:[1,0]
	v_pk_mul_f32 v[66:67], v[66:67], s[18:19] op_sel_hi:[1,0]
	v_pk_mul_f32 v[56:57], v[56:57], s[18:19] op_sel_hi:[1,0]
	v_pk_fma_f32 v[18:19], s[4:5], v[52:53], v[18:19] op_sel_hi:[0,1,1]
	v_pk_mul_f32 v[64:65], v[64:65], s[18:19] op_sel_hi:[1,0]
	v_pk_fma_f32 v[16:17], s[4:5], v[48:49], v[16:17] op_sel_hi:[0,1,1]
	v_pk_fma_f32 v[48:49], s[4:5], v[66:67], v[50:51] op_sel_hi:[0,1,1]
	v_pk_fma_f32 v[44:45], s[4:5], v[56:57], v[44:45] op_sel_hi:[0,1,1]
	v_pk_fma_f32 v[46:47], s[4:5], v[64:65], v[46:47] op_sel_hi:[0,1,1]
	v_cvt_pk_f32_fp8_e32 v[62:63], v55
	v_cvt_pk_f32_fp8_sdwa v[54:55], v55 src0_sel:WORD_1
	v_pk_mul_f32 v[68:69], v[68:69], s[18:19] op_sel_hi:[1,0]
	s_waitcnt vmcnt(0)
; #define GAS __attribute__((address_space(1)))
; #pragma unroll
;     for (int j = 0; j < 4; ++j) s += (v[j].x * v[j].x + v[j].y * v[j].y) + (v[j].z * v[j].z + v[j].w * v[j].w);
;     return rsqrtf(wave_sum(s) * (1.f / DM) + EPSN); }
; __device__ __forceinline__ void phase_e4(Frame& F, int layer, int chunk, int CT, bool dry = false) {
;     ...
;         else if (layer == 0 || !X3_BF16) ldrow_f32_nt(xo, F.lane, x); else ldrow_bf16_nt((const bf16*)xo, F.lane, x);
;         const float ry = rstd_of(y);
; #pragma unroll
;         for (int j = 0; j < 4; ++j) x[j] = x[j] + (y[j] * ry) * C[j];
;         if (layer == 1 && NT_STREAMS) { GAS f32x4* q_ = (GAS f32x4*)xo + F.lane;
; #pragma unroll
;             for (int j = 0; j < 4; ++j) __builtin_nontemporal_store(x[j], q_ + 64 * j); }
;         else strow_f32_nt(xo, F.lane, x);
	v_cvt_pk_f32_fp8_e32 v[66:67], v60
	v_pk_mul_f32 v[62:63], v[62:63], s[18:19] op_sel_hi:[1,0]
	v_pk_mul_f32 v[54:55], v[54:55], s[18:19] op_sel_hi:[1,0]
	v_pk_fma_f32 v[20:21], s[4:5], v[62:63], v[20:21] op_sel_hi:[0,1,1]
	v_pk_fma_f32 v[42:43], s[4:5], v[54:55], v[42:43] op_sel_hi:[0,1,1]
	v_pk_fma_f32 v[22:23], s[4:5], v[68:69], v[22:23] op_sel_hi:[0,1,1]
	v_readfirstlane_b32 s4, v35
	v_cvt_pk_f32_fp8_sdwa v[34:35], v58 src0_sel:WORD_1
	v_cvt_pk_f32_fp8_e32 v[54:55], v58
	v_cvt_pk_f32_fp8_sdwa v[62:63], v59 src0_sel:WORD_1
	v_cvt_pk_f32_fp8_sdwa v[68:69], v60 src0_sel:WORD_1
	v_cvt_pk_f32_fp8_e32 v[70:71], v61
	v_cvt_pk_f32_fp8_sdwa v[60:61], v61 src0_sel:WORD_1
	v_cvt_pk_f32_fp8_e32 v[58:59], v59
	v_pk_mul_f32 v[34:35], v[34:35], s[18:19] op_sel_hi:[1,0]
	v_pk_mul_f32 v[54:55], v[54:55], s[18:19] op_sel_hi:[1,0]
	v_pk_mul_f32 v[62:63], v[62:63], s[18:19] op_sel_hi:[1,0]
	v_pk_mul_f32 v[66:67], v[66:67], s[18:19] op_sel_hi:[1,0]
	v_pk_mul_f32 v[68:69], v[68:69], s[18:19] op_sel_hi:[1,0]
	v_pk_mul_f32 v[70:71], v[70:71], s[18:19] op_sel_hi:[1,0]
	v_pk_mul_f32 v[60:61], v[60:61], s[18:19] op_sel_hi:[1,0]
	v_pk_fma_f32 v[16:17], s[4:5], v[54:55], v[16:17] op_sel_hi:[0,1,1]
	v_pk_fma_f32 v[18:19], s[4:5], v[34:35], v[18:19] op_sel_hi:[0,1,1]
	v_pk_mul_f32 v[58:59], v[58:59], s[18:19] op_sel_hi:[1,0]
	v_pk_fma_f32 v[34:35], s[4:5], v[62:63], v[42:43] op_sel_hi:[0,1,1]
	v_pk_fma_f32 v[42:43], s[4:5], v[68:69], v[46:47] op_sel_hi:[0,1,1]
	v_pk_fma_f32 v[46:47], s[4:5], v[66:67], v[48:49] op_sel_hi:[0,1,1]
	v_pk_fma_f32 v[48:49], s[4:5], v[60:61], v[22:23] op_sel_hi:[0,1,1]
	v_pk_fma_f32 v[54:55], s[4:5], v[70:71], v[44:45] op_sel_hi:[0,1,1]
	v_pk_mul_f32 v[22:23], v[18:19], v[18:19]
	v_pk_mul_f32 v[44:45], v[16:17], v[16:17]
	v_pk_fma_f32 v[20:21], s[4:5], v[58:59], v[20:21] op_sel_hi:[0,1,1]
	v_pk_mov_b32 v[58:59], v[44:45], v[22:23] op_sel:[1,0]
	v_mov_b32_e32 v45, v23
	v_pk_add_f32 v[22:23], v[58:59], v[44:45]
	v_pk_mul_f32 v[44:45], v[34:35], v[34:35]
	v_pk_mul_f32 v[58:59], v[20:21], v[20:21]
	v_mul_f32_e32 v33, v54, v54
	v_pk_mov_b32 v[60:61], v[58:59], v[44:45] op_sel:[1,0]
	v_mov_b32_e32 v59, v45
	v_pk_add_f32 v[44:45], v[60:61], v[58:59]
	v_mul_f32_e32 v58, v55, v55
	v_pk_add_f32 v[22:23], v[22:23], v[22:23] op_sel:[0,1] op_sel_hi:[1,0]
	v_pk_add_f32 v[44:45], v[44:45], v[44:45] op_sel:[0,1] op_sel_hi:[1,0]
	v_mov_b32_e32 v23, v33
	v_mov_b32_e32 v45, v58
	v_pk_add_f32 v[22:23], v[22:23], v[44:45]
	v_mul_f32_e32 v44, v47, v47
	v_mul_f32_e32 v59, v48, v48
	v_pk_fma_f32 v[44:45], v[46:47], v[46:47], v[44:45] op_sel_hi:[1,1,0]
	v_mul_f32_e32 v58, v43, v43
	v_mul_f32_e32 v60, v49, v49
	v_mov_b32_e32 v45, v59
	v_pk_fma_f32 v[58:59], v[42:43], v[42:43], v[58:59] op_sel_hi:[1,1,0]
	s_waitcnt vmcnt(1)
	v_and_b32_e32 v61, 0xffff0000, v124
	v_mov_b32_e32 v59, v60
	v_pk_add_f32 v[44:45], v[44:45], v[58:59]
	v_lshl_add_u64 v[58:59], s[12:13], 0, v[26:27]
	v_pk_add_f32 v[22:23], v[22:23], v[44:45]
	v_lshlrev_b32_e32 v44, 16, v121
	v_add_f32_e32 v22, v22, v23
	ds_bpermute_b32 v23, v25, v22
	v_and_b32_e32 v45, 0xffff0000, v121
	v_lshlrev_b32_e32 v60, 16, v124
	v_lshlrev_b32_e32 v56, 16, v125
	v_and_b32_e32 v57, 0xffff0000, v125
	s_waitcnt lgkmcnt(0)
	v_add_f32_e32 v22, v22, v23
	ds_bpermute_b32 v23, v36, v22
	s_add_u32 s12, s12, 0x1000
	s_waitcnt vmcnt(0)
	v_lshlrev_b32_e32 v62, 16, v126
	v_and_b32_e32 v63, 0xffff0000, v126
	v_lshlrev_b32_e32 v64, 16, v127
	s_waitcnt lgkmcnt(0)
	v_add_f32_e32 v23, v22, v23
	ds_bpermute_b32 v33, v37, v23
	v_lshlrev_b32_e32 v22, 16, v120
	v_and_b32_e32 v65, 0xffff0000, v127
	s_addc_u32 s13, s13, 0
	v_and_b32_e32 v53, 0xffff0000, v122
	s_waitcnt lgkmcnt(0)
	v_add_f32_e32 v26, v23, v33
	ds_bpermute_b32 v33, v38, v26
	v_and_b32_e32 v23, 0xffff0000, v120
	v_lshlrev_b32_e32 v52, 16, v122
	v_lshlrev_b32_e32 v50, 16, v123
	v_and_b32_e32 v51, 0xffff0000, v123
	s_waitcnt lgkmcnt(0)
	v_add_f32_e32 v26, v26, v33
	ds_bpermute_b32 v33, v39, v26
	s_cmp_lt_i32 s2, s19
	s_waitcnt lgkmcnt(0)
	v_add_f32_e32 v26, v26, v33
	ds_bpermute_b32 v33, v40, v26
	s_waitcnt lgkmcnt(0)
	v_add_f32_e32 v26, v26, v33
	v_fmamk_f32 v26, v26, 0x3a800000, v41
	v_mul_f32_e32 v33, 0x4b800000, v26
	v_cmp_gt_f32_e32 vcc, s39, v26
	s_nop 1
	v_cndmask_b32_e32 v26, v26, v33, vcc
	v_rsq_f32_e32 v26, v26
	s_nop 0
	v_mul_f32_e32 v33, 0x45800000, v26
	v_cndmask_b32_e32 v26, v26, v33, vcc
	v_pk_mul_f32 v[16:17], v[16:17], v[26:27] op_sel_hi:[1,0]
	v_pk_mul_f32 v[18:19], v[18:19], v[26:27] op_sel_hi:[1,0]
	v_pk_fma_f32 v[16:17], v[4:5], v[16:17], v[22:23]
	v_pk_mul_f32 v[22:23], v[34:35], v[26:27] op_sel_hi:[1,0]
	v_pk_mul_f32 v[34:35], v[46:47], v[26:27] op_sel_hi:[1,0]
	v_pk_mul_f32 v[42:43], v[42:43], v[26:27] op_sel_hi:[1,0]
	v_pk_fma_f32 v[18:19], v[6:7], v[18:19], v[44:45]
	v_pk_fma_f32 v[44:45], v[10:11], v[42:43], v[56:57]
	v_pk_fma_f32 v[42:43], v[8:9], v[34:35], v[60:61]
	v_pk_mul_f32 v[34:35], v[54:55], v[26:27] op_sel_hi:[1,0]
	v_pk_mul_f32 v[46:47], v[48:49], v[26:27] op_sel_hi:[1,0]
	v_pk_mul_f32 v[20:21], v[20:21], v[26:27] op_sel_hi:[1,0]
	v_pk_fma_f32 v[48:49], v[14:15], v[46:47], v[64:65]
	v_pk_fma_f32 v[46:47], v[12:13], v[34:35], v[62:63]
	v_lshl_add_u64 v[34:35], v[58:59], 0, v[28:29]
	v_pk_fma_f32 v[22:23], v[2:3], v[22:23], v[50:51]
	v_pk_fma_f32 v[20:21], v[0:1], v[20:21], v[52:53]
	global_store_dwordx4 v[34:35], v[16:19], off nt
	global_store_dwordx4 v[34:35], v[20:23], off offset:1024 nt
	global_store_dwordx4 v[34:35], v[42:45], off offset:2048 nt
	global_store_dwordx4 v[34:35], v[46:49], off offset:3072 nt
	s_cbranch_scc0 .LBB0_1812
